# v38: merged-branch GEMM mid-K rescale: touch-prefetch of the gate rows of steps 2..7 right after the first two steps' loads
# baseline (speedup 1.0000x reference)
; #define MG_LOAD(G_, s_) do { const bf16* q_ = pb + (size_t)(((s_) >> 2) * 128 + ((s_) & 3) * 16) * PNP; G_[0] = *(const GAS v4u*)(q_ + PGA); G_[1] = *(const GAS v4u*)(q_ + PGB); G_[2] = *(const GAS v4u*)(q_ + PGA + 128); G_[3] = *(const GAS v4u*)(q_ + PGB + 128); } while (0)
;     __device__ __forceinline__ void mid(f32x4 (&acc)[2][2][4][2], const Unit& u, int wr, int wc, int fr, int fq) const {
;         const bf16* pb = P + (size_t)(u.pm * 256 + wr * 64 + fr) * PNP + (u.pn * 256 + wc * 32 + 8 * fq);
;         asm volatile("" : "+v"(pb));
;         v4u A0[4], A1[4];
;     ...
;         MG_LOAD(A0, 0); MG_LOAD(A1, 1); MG_APPLY(A0, 0); MG_LOAD(A0, 2); MG_APPLY(A1, 1); MG_LOAD(A1, 3); MG_APPLY(A0, 2); MG_LOAD(A0, 4); MG_APPLY(A1, 3); MG_LOAD(A1, 5);
;         MG_APPLY(A0, 4); MG_LOAD(A0, 6); MG_APPLY(A1, 5); MG_LOAD(A1, 7); MG_APPLY(A0, 6); MG_APPLY(A1, 7);
.LBB0_1709:
	s_cmpk_lg_i32 s30, 0x800
	s_cbranch_scc1 .LBB0_1708
	v_mov_b64_e32 v[28:29], v[204:205]
	s_nop 15
	s_nop 15
	s_mov_b32 s34, 0x118000
	v_add_co_u32_e32 v2, vcc, 0x4000, v28
	s_nop 1
	v_addc_co_u32_e32 v3, vcc, 0, v29, vcc
	v_add_co_u32_e32 v4, vcc, 0x6000, v28
	global_load_dwordx4 v[158:161], v[2:3], off offset:2048
	s_nop 0
	v_addc_co_u32_e32 v5, vcc, 0, v29, vcc
	global_load_dwordx4 v[162:165], v[4:5], off offset:2048
	global_load_dwordx4 v[18:21], v[2:3], off offset:2304
	global_load_dwordx4 v[22:25], v[4:5], off offset:2304
	v_add_co_u32_e32 v2, vcc, 0x8e000, v28
	s_waitcnt vmcnt(3)
	v_lshlrev_b32_e32 v168, 16, v158
	v_addc_co_u32_e32 v3, vcc, 0, v29, vcc
	global_load_dwordx4 v[10:13], v[2:3], off offset:2048
	v_add_co_u32_e32 v6, vcc, 0x90000, v28
	s_waitcnt vmcnt(3)
	v_lshlrev_b32_e32 v27, 16, v162
	s_nop 0
	v_addc_co_u32_e32 v7, vcc, 0, v29, vcc
	global_load_dwordx4 v[14:17], v[6:7], off offset:2048
	s_nop 0
	global_load_dwordx4 v[2:5], v[2:3], off offset:2304
	s_nop 0
	global_load_dwordx4 v[6:9], v[6:7], off offset:2304
	s_mov_b64 s[36:37], 0x118000
	v_lshl_add_u64 v[210:211], v[28:29], 0, s[36:37]
	global_load_dword v212, v[210:211], off offset:2048
	global_load_dword v213, v[210:211], off offset:2304
	s_mov_b64 s[36:37], 0x11a000
	v_lshl_add_u64 v[210:211], v[28:29], 0, s[36:37]
	global_load_dword v214, v[210:211], off offset:2048
	global_load_dword v215, v[210:211], off offset:2304
	s_mov_b64 s[36:37], 0x1a2000
	v_lshl_add_u64 v[210:211], v[28:29], 0, s[36:37]
	global_load_dword v216, v[210:211], off offset:2048
	global_load_dword v217, v[210:211], off offset:2304
	s_mov_b64 s[36:37], 0x1a4000
	v_lshl_add_u64 v[210:211], v[28:29], 0, s[36:37]
	global_load_dword v218, v[210:211], off offset:2048
	global_load_dword v219, v[210:211], off offset:2304
	s_mov_b64 s[36:37], 0x454000
	v_lshl_add_u64 v[210:211], v[28:29], 0, s[36:37]
	global_load_dword v220, v[210:211], off offset:2048
	global_load_dword v221, v[210:211], off offset:2304
	s_mov_b64 s[36:37], 0x456000
	v_lshl_add_u64 v[210:211], v[28:29], 0, s[36:37]
	global_load_dword v222, v[210:211], off offset:2048
	global_load_dword v223, v[210:211], off offset:2304
	s_mov_b64 s[36:37], 0x4de000
	v_lshl_add_u64 v[210:211], v[28:29], 0, s[36:37]
	global_load_dword v224, v[210:211], off offset:2048
	global_load_dword v225, v[210:211], off offset:2304
	s_mov_b64 s[36:37], 0x4e0000
	v_lshl_add_u64 v[210:211], v[28:29], 0, s[36:37]
	global_load_dword v226, v[210:211], off offset:2048
	global_load_dword v227, v[210:211], off offset:2304
	s_mov_b64 s[36:37], 0x568000
	v_lshl_add_u64 v[210:211], v[28:29], 0, s[36:37]
	global_load_dword v228, v[210:211], off offset:2048
	global_load_dword v229, v[210:211], off offset:2304
	s_mov_b64 s[36:37], 0x56a000
	v_lshl_add_u64 v[210:211], v[28:29], 0, s[36:37]
	global_load_dword v230, v[210:211], off offset:2048
	global_load_dword v231, v[210:211], off offset:2304
	s_mov_b64 s[36:37], 0x5f2000
	v_lshl_add_u64 v[210:211], v[28:29], 0, s[36:37]
	global_load_dword v232, v[210:211], off offset:2048
	global_load_dword v233, v[210:211], off offset:2304
	s_mov_b64 s[36:37], 0x5f4000
	v_lshl_add_u64 v[210:211], v[28:29], 0, s[36:37]
	global_load_dword v234, v[210:211], off offset:2048
	global_load_dword v235, v[210:211], off offset:2304
	v_max_f32_e32 v27, v27, v27
	v_max_f32_e32 v27, 0xda24260, v27
	v_rcp_f32_e32 v166, v27
	v_and_b32_e32 v27, 0xffff0000, v162
	v_max_f32_e32 v27, v27, v27
	v_max_f32_e32 v27, 0xda24260, v27
	v_rcp_f32_e32 v167, v27
	v_lshlrev_b32_e32 v27, 16, v163
	v_max_f32_e32 v27, v27, v27
	v_max_f32_e32 v27, 0xda24260, v27
	v_rcp_f32_e32 v162, v27
	v_and_b32_e32 v27, 0xffff0000, v163
	v_max_f32_e32 v27, v27, v27
	v_max_f32_e32 v27, 0xda24260, v27
	v_rcp_f32_e32 v163, v27
	v_and_b32_e32 v169, 0xffff0000, v158
	v_lshlrev_b32_e32 v158, 16, v159
	v_and_b32_e32 v159, 0xffff0000, v159
	v_lshlrev_b32_e32 v27, 16, v164
	v_pk_mul_f32 v[158:159], v[158:159], 0.5 op_sel_hi:[1,0]
	v_max_f32_e32 v27, v27, v27
	v_pk_mul_f32 v[158:159], v[158:159], v[162:163]
	v_max_f32_e32 v27, 0xda24260, v27
	v_pk_mul_f32 v[156:157], v[156:157], v[158:159]
	v_rcp_f32_e32 v158, v27
	v_and_b32_e32 v27, 0xffff0000, v164
	v_max_f32_e32 v27, v27, v27
	v_max_f32_e32 v27, 0xda24260, v27
	v_rcp_f32_e32 v159, v27
	v_lshlrev_b32_e32 v27, 16, v165
	v_lshlrev_b32_e32 v162, 16, v160
	v_and_b32_e32 v163, 0xffff0000, v160
	v_max_f32_e32 v27, v27, v27
	v_pk_mul_f32 v[162:163], v[162:163], 0.5 op_sel_hi:[1,0]
	v_max_f32_e32 v27, 0xda24260, v27
	v_pk_mul_f32 v[158:159], v[162:163], v[158:159]
	v_rcp_f32_e32 v162, v27
	v_and_b32_e32 v27, 0xffff0000, v165
	v_max_f32_e32 v27, v27, v27
	v_max_f32_e32 v27, 0xda24260, v27
	v_rcp_f32_e32 v163, v27
	v_lshlrev_b32_e32 v160, 16, v161
	v_and_b32_e32 v161, 0xffff0000, v161
	v_pk_mul_f32 v[160:161], v[160:161], 0.5 op_sel_hi:[1,0]
	s_waitcnt vmcnt(28)
	v_lshlrev_b32_e32 v27, 16, v22
	v_pk_mul_f32 v[160:161], v[160:161], v[162:163]
	v_and_b32_e32 v22, 0xffff0000, v22
	v_pk_mul_f32 v[152:153], v[152:153], v[160:161]
	v_lshlrev_b32_e32 v160, 16, v18
	v_and_b32_e32 v161, 0xffff0000, v18
	v_lshlrev_b32_e32 v18, 16, v23
	v_max_f32_e32 v22, v22, v22
	v_max_f32_e32 v18, v18, v18
	v_max_f32_e32 v22, 0xda24260, v22
	v_max_f32_e32 v18, 0xda24260, v18
	v_pk_mul_f32 v[150:151], v[150:151], v[158:159]
	v_rcp_f32_e32 v159, v22
	v_rcp_f32_e32 v22, v18
	v_and_b32_e32 v18, 0xffff0000, v23
	v_max_f32_e32 v18, v18, v18
	v_max_f32_e32 v18, 0xda24260, v18
	v_rcp_f32_e32 v23, v18
	v_lshlrev_b32_e32 v18, 16, v19
	v_and_b32_e32 v19, 0xffff0000, v19
	v_pk_mul_f32 v[18:19], v[18:19], 0.5 op_sel_hi:[1,0]
	v_max_f32_e32 v27, v27, v27
	v_pk_mul_f32 v[18:19], v[18:19], v[22:23]
	v_max_f32_e32 v27, 0xda24260, v27
	v_pk_mul_f32 v[148:149], v[148:149], v[18:19]
	v_lshlrev_b32_e32 v18, 16, v24
	v_and_b32_e32 v19, 0xffff0000, v24
	v_max_f32_e32 v18, v18, v18
	v_max_f32_e32 v19, v19, v19
	v_max_f32_e32 v18, 0xda24260, v18
	v_max_f32_e32 v19, 0xda24260, v19
	v_rcp_f32_e32 v18, v18
	v_rcp_f32_e32 v19, v19
	v_rcp_f32_e32 v158, v27
	v_lshlrev_b32_e32 v22, 16, v20
	v_and_b32_e32 v23, 0xffff0000, v20
	v_lshlrev_b32_e32 v20, 16, v25
	s_waitcnt vmcnt(26)
; #define MG_LOAD(G_, s_) do { const bf16* q_ = pb + (size_t)(((s_) >> 2) * 128 + ((s_) & 3) * 16) * PNP; G_[0] = *(const GAS v4u*)(q_ + PGA); G_[1] = *(const GAS v4u*)(q_ + PGB); G_[2] = *(const GAS v4u*)(q_ + PGA + 128); G_[3] = *(const GAS v4u*)(q_ + PGB + 128); } while (0)
;     __device__ __forceinline__ void mid(f32x4 (&acc)[2][2][4][2], const Unit& u, int wr, int wc, int fr, int fq) const {
;     ...
;         MG_LOAD(A0, 0); MG_LOAD(A1, 1); MG_APPLY(A0, 0); MG_LOAD(A0, 2); MG_APPLY(A1, 1); MG_LOAD(A1, 3); MG_APPLY(A0, 2); MG_LOAD(A0, 4); MG_APPLY(A1, 3); MG_LOAD(A1, 5);
;         MG_APPLY(A0, 4); MG_LOAD(A0, 6); MG_APPLY(A1, 5); MG_LOAD(A1, 7); MG_APPLY(A0, 6); MG_APPLY(A1, 7);
	v_lshlrev_b32_e32 v27, 16, v14
	v_and_b32_e32 v14, 0xffff0000, v14
	v_lshlrev_b32_e32 v164, 16, v10
	v_and_b32_e32 v165, 0xffff0000, v10
	v_lshlrev_b32_e32 v10, 16, v15
	v_max_f32_e32 v20, v20, v20
	v_max_f32_e32 v14, v14, v14
	v_max_f32_e32 v10, v10, v10
	v_pk_mul_f32 v[22:23], v[22:23], 0.5 op_sel_hi:[1,0]
	v_max_f32_e32 v20, 0xda24260, v20
	v_max_f32_e32 v14, 0xda24260, v14
	v_max_f32_e32 v10, 0xda24260, v10
	v_pk_mul_f32 v[18:19], v[22:23], v[18:19]
	v_rcp_f32_e32 v22, v20
	v_and_b32_e32 v20, 0xffff0000, v25
	v_rcp_f32_e32 v163, v14
	v_rcp_f32_e32 v14, v10
	v_and_b32_e32 v10, 0xffff0000, v15
	v_max_f32_e32 v20, v20, v20
	v_max_f32_e32 v10, v10, v10
	v_max_f32_e32 v20, 0xda24260, v20
	v_max_f32_e32 v10, 0xda24260, v10
	v_rcp_f32_e32 v23, v20
	v_rcp_f32_e32 v15, v10
	v_lshlrev_b32_e32 v20, 16, v21
	v_and_b32_e32 v21, 0xffff0000, v21
	v_pk_mul_f32 v[142:143], v[142:143], v[18:19]
	v_add_co_u32_e32 v18, vcc, s34, v28
	v_lshlrev_b32_e32 v10, 16, v11
	v_and_b32_e32 v11, 0xffff0000, v11
	v_pk_mul_f32 v[20:21], v[20:21], 0.5 op_sel_hi:[1,0]
	v_addc_co_u32_e32 v19, vcc, 0, v29, vcc
	s_mov_b32 s34, 0x11a000
	v_pk_mul_f32 v[10:11], v[10:11], 0.5 op_sel_hi:[1,0]
	v_pk_mul_f32 v[168:169], v[168:169], 0.5 op_sel_hi:[1,0]
	v_pk_mul_f32 v[160:161], v[160:161], 0.5 op_sel_hi:[1,0]
	v_pk_mul_f32 v[20:21], v[20:21], v[22:23]
	v_add_co_u32_e32 v22, vcc, s34, v28
	v_pk_mul_f32 v[10:11], v[10:11], v[14:15]
	v_pk_mul_f32 v[166:167], v[168:169], v[166:167]
	v_pk_mul_f32 v[158:159], v[160:161], v[158:159]
	v_addc_co_u32_e32 v23, vcc, 0, v29, vcc
	v_pk_mul_f32 v[140:141], v[140:141], v[10:11]
	v_lshlrev_b32_e32 v10, 16, v16
	v_and_b32_e32 v11, 0xffff0000, v16
	v_pk_mul_f32 v[154:155], v[154:155], v[166:167]
	v_pk_mul_f32 v[146:147], v[146:147], v[158:159]
	v_pk_mul_f32 v[144:145], v[144:145], v[20:21]
	global_load_dwordx4 v[158:161], v[18:19], off offset:2048
	global_load_dwordx4 v[166:169], v[22:23], off offset:2048
	s_nop 0
	global_load_dwordx4 v[18:21], v[18:19], off offset:2304
	s_nop 0
	global_load_dwordx4 v[22:25], v[22:23], off offset:2304
	v_max_f32_e32 v10, v10, v10
	v_max_f32_e32 v11, v11, v11
	v_max_f32_e32 v10, 0xda24260, v10
	v_max_f32_e32 v11, 0xda24260, v11
	v_rcp_f32_e32 v10, v10
	v_rcp_f32_e32 v11, v11
	v_lshlrev_b32_e32 v14, 16, v12
	v_and_b32_e32 v15, 0xffff0000, v12
	v_lshlrev_b32_e32 v12, 16, v17
	v_max_f32_e32 v12, v12, v12
	v_pk_mul_f32 v[14:15], v[14:15], 0.5 op_sel_hi:[1,0]
	v_max_f32_e32 v12, 0xda24260, v12
	v_pk_mul_f32 v[10:11], v[14:15], v[10:11]
	v_rcp_f32_e32 v14, v12
	v_and_b32_e32 v12, 0xffff0000, v17
	v_max_f32_e32 v12, v12, v12
	v_max_f32_e32 v12, 0xda24260, v12
	v_rcp_f32_e32 v15, v12
	v_lshlrev_b32_e32 v12, 16, v13
	v_and_b32_e32 v13, 0xffff0000, v13
	v_pk_mul_f32 v[12:13], v[12:13], 0.5 op_sel_hi:[1,0]
	v_pk_mul_f32 v[134:135], v[134:135], v[10:11]
	v_pk_mul_f32 v[12:13], v[12:13], v[14:15]
	s_waitcnt vmcnt(28)
	v_lshlrev_b32_e32 v10, 16, v6
	v_pk_mul_f32 v[136:137], v[136:137], v[12:13]
	v_and_b32_e32 v6, 0xffff0000, v6
	v_lshlrev_b32_e32 v12, 16, v2
	v_and_b32_e32 v13, 0xffff0000, v2
	v_lshlrev_b32_e32 v2, 16, v7
	v_max_f32_e32 v6, v6, v6
	v_max_f32_e32 v2, v2, v2
	v_max_f32_e32 v6, 0xda24260, v6
	v_max_f32_e32 v2, 0xda24260, v2
	v_rcp_f32_e32 v11, v6
	v_rcp_f32_e32 v6, v2
	v_and_b32_e32 v2, 0xffff0000, v7
	v_max_f32_e32 v2, v2, v2
	v_max_f32_e32 v2, 0xda24260, v2
	v_rcp_f32_e32 v7, v2
	v_lshlrev_b32_e32 v2, 16, v3
	v_and_b32_e32 v3, 0xffff0000, v3
	v_pk_mul_f32 v[2:3], v[2:3], 0.5 op_sel_hi:[1,0]
	v_max_f32_e32 v27, v27, v27
	v_pk_mul_f32 v[2:3], v[2:3], v[6:7]
	v_lshlrev_b32_e32 v6, 16, v4
	v_pk_mul_f32 v[132:133], v[132:133], v[2:3]
	v_lshlrev_b32_e32 v2, 16, v8
	v_and_b32_e32 v3, 0xffff0000, v8
	v_max_f32_e32 v2, v2, v2
	v_max_f32_e32 v3, v3, v3
	v_max_f32_e32 v2, 0xda24260, v2
	v_max_f32_e32 v3, 0xda24260, v3
	v_rcp_f32_e32 v2, v2
	v_rcp_f32_e32 v3, v3
	v_and_b32_e32 v7, 0xffff0000, v4
	v_lshlrev_b32_e32 v4, 16, v9
	v_max_f32_e32 v4, v4, v4
	v_pk_mul_f32 v[6:7], v[6:7], 0.5 op_sel_hi:[1,0]
	v_max_f32_e32 v4, 0xda24260, v4
	v_pk_mul_f32 v[2:3], v[6:7], v[2:3]
	v_rcp_f32_e32 v6, v4
	v_and_b32_e32 v4, 0xffff0000, v9
	v_max_f32_e32 v4, v4, v4
	v_max_f32_e32 v10, v10, v10
	v_max_f32_e32 v4, 0xda24260, v4
	v_max_f32_e32 v27, 0xda24260, v27
	v_max_f32_e32 v10, 0xda24260, v10
	v_rcp_f32_e32 v7, v4
	v_rcp_f32_e32 v162, v27
	v_rcp_f32_e32 v10, v10
	s_mov_b32 s34, 0x1a2000
	v_lshlrev_b32_e32 v4, 16, v5
	v_and_b32_e32 v5, 0xffff0000, v5
	v_pk_mul_f32 v[126:127], v[126:127], v[2:3]
	v_add_co_u32_e32 v2, vcc, s34, v28
	v_pk_mul_f32 v[4:5], v[4:5], 0.5 op_sel_hi:[1,0]
	s_nop 0
	v_addc_co_u32_e32 v3, vcc, 0, v29, vcc
	s_mov_b32 s34, 0x1a4000
	v_pk_mul_f32 v[164:165], v[164:165], 0.5 op_sel_hi:[1,0]
	v_pk_mul_f32 v[12:13], v[12:13], 0.5 op_sel_hi:[1,0]
	v_pk_mul_f32 v[4:5], v[4:5], v[6:7]
	v_add_co_u32_e32 v6, vcc, s34, v28
	v_pk_mul_f32 v[162:163], v[164:165], v[162:163]
	v_pk_mul_f32 v[10:11], v[12:13], v[10:11]
	v_addc_co_u32_e32 v7, vcc, 0, v29, vcc
	v_pk_mul_f32 v[138:139], v[138:139], v[162:163]
	v_pk_mul_f32 v[130:131], v[130:131], v[10:11]
	v_pk_mul_f32 v[128:129], v[128:129], v[4:5]
	global_load_dwordx4 v[162:165], v[2:3], off offset:2048
	global_load_dwordx4 v[170:173], v[6:7], off offset:2048
	s_nop 0
	global_load_dwordx4 v[2:5], v[2:3], off offset:2304
	s_nop 0
	global_load_dwordx4 v[10:13], v[6:7], off offset:2304
	s_waitcnt vmcnt(6)
; #define MG_LOAD(G_, s_) do { const bf16* q_ = pb + (size_t)(((s_) >> 2) * 128 + ((s_) & 3) * 16) * PNP; G_[0] = *(const GAS v4u*)(q_ + PGA); G_[1] = *(const GAS v4u*)(q_ + PGB); G_[2] = *(const GAS v4u*)(q_ + PGA + 128); G_[3] = *(const GAS v4u*)(q_ + PGB + 128); } while (0)
;     __device__ __forceinline__ void mid(f32x4 (&acc)[2][2][4][2], const Unit& u, int wr, int wc, int fr, int fq) const {
;     ...
;         MG_LOAD(A0, 0); MG_LOAD(A1, 1); MG_APPLY(A0, 0); MG_LOAD(A0, 2); MG_APPLY(A1, 1); MG_LOAD(A1, 3); MG_APPLY(A0, 2); MG_LOAD(A0, 4); MG_APPLY(A1, 3); MG_LOAD(A1, 5);
;         MG_APPLY(A0, 4); MG_LOAD(A0, 6); MG_APPLY(A1, 5); MG_LOAD(A1, 7); MG_APPLY(A0, 6); MG_APPLY(A1, 7);
	v_lshlrev_b32_e32 v6, 16, v166
	v_and_b32_e32 v7, 0xffff0000, v166
	v_max_f32_e32 v6, v6, v6
	v_max_f32_e32 v7, v7, v7
	v_max_f32_e32 v6, 0xda24260, v6
	v_max_f32_e32 v7, 0xda24260, v7
	v_rcp_f32_e32 v6, v6
	v_rcp_f32_e32 v7, v7
	v_lshlrev_b32_e32 v8, 16, v158
	v_and_b32_e32 v9, 0xffff0000, v158
	v_pk_mul_f32 v[8:9], v[8:9], 0.5 op_sel_hi:[1,0]
	v_lshlrev_b32_e32 v14, 16, v159
	v_pk_mul_f32 v[6:7], v[8:9], v[6:7]
	v_lshlrev_b32_e32 v8, 16, v167
	v_and_b32_e32 v9, 0xffff0000, v167
	v_max_f32_e32 v8, v8, v8
	v_max_f32_e32 v9, v9, v9
	v_max_f32_e32 v8, 0xda24260, v8
	v_max_f32_e32 v9, 0xda24260, v9
	v_rcp_f32_e32 v8, v8
	v_rcp_f32_e32 v9, v9
	v_pk_mul_f32 v[122:123], v[122:123], v[6:7]
	v_lshlrev_b32_e32 v6, 16, v168
	v_and_b32_e32 v7, 0xffff0000, v168
	v_max_f32_e32 v6, v6, v6
	v_max_f32_e32 v7, v7, v7
	v_and_b32_e32 v15, 0xffff0000, v159
	v_max_f32_e32 v6, 0xda24260, v6
	v_max_f32_e32 v7, 0xda24260, v7
	v_pk_mul_f32 v[14:15], v[14:15], 0.5 op_sel_hi:[1,0]
	v_rcp_f32_e32 v6, v6
	v_rcp_f32_e32 v7, v7
	v_pk_mul_f32 v[8:9], v[14:15], v[8:9]
	v_lshlrev_b32_e32 v14, 16, v161
	v_pk_mul_f32 v[124:125], v[124:125], v[8:9]
	v_lshlrev_b32_e32 v8, 16, v160
	v_and_b32_e32 v9, 0xffff0000, v160
	v_pk_mul_f32 v[8:9], v[8:9], 0.5 op_sel_hi:[1,0]
	v_and_b32_e32 v15, 0xffff0000, v161
	v_pk_mul_f32 v[6:7], v[8:9], v[6:7]
	v_lshlrev_b32_e32 v8, 16, v169
	v_and_b32_e32 v9, 0xffff0000, v169
	v_max_f32_e32 v8, v8, v8
	v_max_f32_e32 v9, v9, v9
	v_max_f32_e32 v8, 0xda24260, v8
	v_max_f32_e32 v9, 0xda24260, v9
	v_rcp_f32_e32 v8, v8
	v_rcp_f32_e32 v9, v9
	v_pk_mul_f32 v[118:119], v[118:119], v[6:7]
	s_waitcnt vmcnt(4)
	v_lshlrev_b32_e32 v6, 16, v22
	v_and_b32_e32 v7, 0xffff0000, v22
	v_max_f32_e32 v6, v6, v6
	v_max_f32_e32 v7, v7, v7
	v_max_f32_e32 v6, 0xda24260, v6
	v_max_f32_e32 v7, 0xda24260, v7
	v_pk_mul_f32 v[14:15], v[14:15], 0.5 op_sel_hi:[1,0]
	v_rcp_f32_e32 v6, v6
	v_rcp_f32_e32 v7, v7
	v_pk_mul_f32 v[8:9], v[14:15], v[8:9]
	v_lshlrev_b32_e32 v14, 16, v19
	v_pk_mul_f32 v[120:121], v[120:121], v[8:9]
	v_lshlrev_b32_e32 v8, 16, v18
	v_and_b32_e32 v9, 0xffff0000, v18
	v_pk_mul_f32 v[8:9], v[8:9], 0.5 op_sel_hi:[1,0]
	v_and_b32_e32 v15, 0xffff0000, v19
	v_pk_mul_f32 v[6:7], v[8:9], v[6:7]
	v_lshlrev_b32_e32 v8, 16, v23
	v_and_b32_e32 v9, 0xffff0000, v23
	v_max_f32_e32 v8, v8, v8
	v_max_f32_e32 v9, v9, v9
	v_max_f32_e32 v8, 0xda24260, v8
	v_max_f32_e32 v9, 0xda24260, v9
	v_rcp_f32_e32 v8, v8
	v_rcp_f32_e32 v9, v9
	v_pk_mul_f32 v[114:115], v[114:115], v[6:7]
	v_lshlrev_b32_e32 v6, 16, v24
	v_and_b32_e32 v7, 0xffff0000, v24
	v_max_f32_e32 v6, v6, v6
	v_max_f32_e32 v7, v7, v7
	v_max_f32_e32 v6, 0xda24260, v6
	v_max_f32_e32 v7, 0xda24260, v7
	v_pk_mul_f32 v[14:15], v[14:15], 0.5 op_sel_hi:[1,0]
	v_rcp_f32_e32 v6, v6
	v_rcp_f32_e32 v7, v7
	v_pk_mul_f32 v[8:9], v[14:15], v[8:9]
	s_mov_b32 s34, 0x454000
	v_pk_mul_f32 v[116:117], v[116:117], v[8:9]
	v_lshlrev_b32_e32 v8, 16, v20
	v_and_b32_e32 v9, 0xffff0000, v20
	v_pk_mul_f32 v[8:9], v[8:9], 0.5 op_sel_hi:[1,0]
	s_waitcnt vmcnt(2)
	v_lshlrev_b32_e32 v22, 16, v170
	v_pk_mul_f32 v[6:7], v[8:9], v[6:7]
	v_lshlrev_b32_e32 v8, 16, v25
	v_and_b32_e32 v9, 0xffff0000, v25
	v_max_f32_e32 v8, v8, v8
	v_max_f32_e32 v9, v9, v9
	v_max_f32_e32 v8, 0xda24260, v8
	v_max_f32_e32 v9, 0xda24260, v9
	v_rcp_f32_e32 v8, v8
	v_rcp_f32_e32 v9, v9
	v_and_b32_e32 v23, 0xffff0000, v170
	v_lshlrev_b32_e32 v14, 16, v21
	v_and_b32_e32 v15, 0xffff0000, v21
	v_pk_mul_f32 v[110:111], v[110:111], v[6:7]
	v_add_co_u32_e32 v6, vcc, s34, v28
	v_max_f32_e32 v22, v22, v22
	v_max_f32_e32 v23, v23, v23
	v_pk_mul_f32 v[14:15], v[14:15], 0.5 op_sel_hi:[1,0]
	v_addc_co_u32_e32 v7, vcc, 0, v29, vcc
	s_mov_b32 s34, 0x456000
	v_max_f32_e32 v22, 0xda24260, v22
	v_max_f32_e32 v23, 0xda24260, v23
	v_pk_mul_f32 v[8:9], v[14:15], v[8:9]
	global_load_dwordx4 v[18:21], v[6:7], off offset:2048
	v_add_co_u32_e32 v14, vcc, s34, v28
	v_rcp_f32_e32 v22, v22
	v_rcp_f32_e32 v23, v23
	v_addc_co_u32_e32 v15, vcc, 0, v29, vcc
	v_pk_mul_f32 v[112:113], v[112:113], v[8:9]
	global_load_dwordx4 v[158:161], v[14:15], off offset:2048
	s_nop 0
	global_load_dwordx4 v[6:9], v[6:7], off offset:2304
	s_nop 0
	global_load_dwordx4 v[14:17], v[14:15], off offset:2304
	v_lshlrev_b32_e32 v24, 16, v162
	v_and_b32_e32 v25, 0xffff0000, v162
	v_pk_mul_f32 v[24:25], v[24:25], 0.5 op_sel_hi:[1,0]
	v_lshlrev_b32_e32 v162, 16, v163
	v_pk_mul_f32 v[22:23], v[24:25], v[22:23]
	v_lshlrev_b32_e32 v24, 16, v171
	v_and_b32_e32 v25, 0xffff0000, v171
	v_max_f32_e32 v24, v24, v24
	v_max_f32_e32 v25, v25, v25
	v_max_f32_e32 v24, 0xda24260, v24
	v_max_f32_e32 v25, 0xda24260, v25
	v_rcp_f32_e32 v24, v24
	v_rcp_f32_e32 v25, v25
	v_pk_mul_f32 v[106:107], v[106:107], v[22:23]
	v_lshlrev_b32_e32 v22, 16, v172
	v_and_b32_e32 v23, 0xffff0000, v172
	v_max_f32_e32 v22, v22, v22
	v_max_f32_e32 v23, v23, v23
	v_and_b32_e32 v163, 0xffff0000, v163
	v_max_f32_e32 v22, 0xda24260, v22
	v_max_f32_e32 v23, 0xda24260, v23
	v_pk_mul_f32 v[162:163], v[162:163], 0.5 op_sel_hi:[1,0]
	v_rcp_f32_e32 v22, v22
	v_rcp_f32_e32 v23, v23
	v_pk_mul_f32 v[24:25], v[162:163], v[24:25]
	v_lshlrev_b32_e32 v162, 16, v165
	v_pk_mul_f32 v[108:109], v[108:109], v[24:25]
	v_lshlrev_b32_e32 v24, 16, v164
	v_and_b32_e32 v25, 0xffff0000, v164
	v_pk_mul_f32 v[24:25], v[24:25], 0.5 op_sel_hi:[1,0]
	v_and_b32_e32 v163, 0xffff0000, v165
	v_pk_mul_f32 v[22:23], v[24:25], v[22:23]
	v_lshlrev_b32_e32 v24, 16, v173
	v_and_b32_e32 v25, 0xffff0000, v173
	v_max_f32_e32 v24, v24, v24
	v_max_f32_e32 v25, v25, v25
	v_max_f32_e32 v24, 0xda24260, v24
	v_max_f32_e32 v25, 0xda24260, v25
	v_rcp_f32_e32 v24, v24
	v_rcp_f32_e32 v25, v25
	v_pk_mul_f32 v[162:163], v[162:163], 0.5 op_sel_hi:[1,0]
	v_pk_mul_f32 v[102:103], v[102:103], v[22:23]
	s_waitcnt vmcnt(4)
; #define MG_LOAD(G_, s_) do { const bf16* q_ = pb + (size_t)(((s_) >> 2) * 128 + ((s_) & 3) * 16) * PNP; G_[0] = *(const GAS v4u*)(q_ + PGA); G_[1] = *(const GAS v4u*)(q_ + PGB); G_[2] = *(const GAS v4u*)(q_ + PGA + 128); G_[3] = *(const GAS v4u*)(q_ + PGB + 128); } while (0)
;     __device__ __forceinline__ void mid(f32x4 (&acc)[2][2][4][2], const Unit& u, int wr, int wc, int fr, int fq) const {
;     ...
;         MG_LOAD(A0, 0); MG_LOAD(A1, 1); MG_APPLY(A0, 0); MG_LOAD(A0, 2); MG_APPLY(A1, 1); MG_LOAD(A1, 3); MG_APPLY(A0, 2); MG_LOAD(A0, 4); MG_APPLY(A1, 3); MG_LOAD(A1, 5);
;         MG_APPLY(A0, 4); MG_LOAD(A0, 6); MG_APPLY(A1, 5); MG_LOAD(A1, 7); MG_APPLY(A0, 6); MG_APPLY(A1, 7);
	v_lshlrev_b32_e32 v22, 16, v10
	v_pk_mul_f32 v[24:25], v[162:163], v[24:25]
	v_and_b32_e32 v10, 0xffff0000, v10
	v_pk_mul_f32 v[104:105], v[104:105], v[24:25]
	v_lshlrev_b32_e32 v24, 16, v2
	v_and_b32_e32 v25, 0xffff0000, v2
	v_lshlrev_b32_e32 v2, 16, v11
	v_max_f32_e32 v10, v10, v10
	v_max_f32_e32 v2, v2, v2
	v_max_f32_e32 v10, 0xda24260, v10
	v_max_f32_e32 v2, 0xda24260, v2
	v_rcp_f32_e32 v23, v10
	v_rcp_f32_e32 v10, v2
	v_and_b32_e32 v2, 0xffff0000, v11
	v_max_f32_e32 v2, v2, v2
	v_max_f32_e32 v2, 0xda24260, v2
	v_rcp_f32_e32 v11, v2
	v_lshlrev_b32_e32 v2, 16, v3
	v_and_b32_e32 v3, 0xffff0000, v3
	v_pk_mul_f32 v[2:3], v[2:3], 0.5 op_sel_hi:[1,0]
	v_max_f32_e32 v22, v22, v22
	v_pk_mul_f32 v[2:3], v[2:3], v[10:11]
	v_lshlrev_b32_e32 v10, 16, v4
	v_pk_mul_f32 v[100:101], v[100:101], v[2:3]
	v_lshlrev_b32_e32 v2, 16, v12
	v_and_b32_e32 v3, 0xffff0000, v12
	v_max_f32_e32 v2, v2, v2
	v_max_f32_e32 v3, v3, v3
	v_max_f32_e32 v2, 0xda24260, v2
	v_max_f32_e32 v3, 0xda24260, v3
	v_rcp_f32_e32 v2, v2
	v_rcp_f32_e32 v3, v3
	v_and_b32_e32 v11, 0xffff0000, v4
	v_lshlrev_b32_e32 v4, 16, v13
	v_max_f32_e32 v4, v4, v4
	v_pk_mul_f32 v[10:11], v[10:11], 0.5 op_sel_hi:[1,0]
	v_max_f32_e32 v4, 0xda24260, v4
	v_pk_mul_f32 v[2:3], v[10:11], v[2:3]
	v_rcp_f32_e32 v10, v4
	v_and_b32_e32 v4, 0xffff0000, v13
	v_max_f32_e32 v22, 0xda24260, v22
	v_max_f32_e32 v4, v4, v4
	v_rcp_f32_e32 v22, v22
	v_max_f32_e32 v4, 0xda24260, v4
	v_rcp_f32_e32 v11, v4
	s_mov_b32 s34, 0x4de000
	v_pk_mul_f32 v[24:25], v[24:25], 0.5 op_sel_hi:[1,0]
	v_lshlrev_b32_e32 v4, 16, v5
	v_and_b32_e32 v5, 0xffff0000, v5
	v_pk_mul_f32 v[94:95], v[94:95], v[2:3]
	v_add_co_u32_e32 v2, vcc, s34, v28
	v_pk_mul_f32 v[22:23], v[24:25], v[22:23]
	v_pk_mul_f32 v[4:5], v[4:5], 0.5 op_sel_hi:[1,0]
	v_addc_co_u32_e32 v3, vcc, 0, v29, vcc
	s_mov_b32 s34, 0x4e0000
	v_pk_mul_f32 v[98:99], v[98:99], v[22:23]
	v_pk_mul_f32 v[4:5], v[4:5], v[10:11]
	global_load_dwordx4 v[22:25], v[2:3], off offset:2048
	v_add_co_u32_e32 v10, vcc, s34, v28
	v_pk_mul_f32 v[96:97], v[96:97], v[4:5]
	s_nop 0
	v_addc_co_u32_e32 v11, vcc, 0, v29, vcc
	global_load_dwordx4 v[162:165], v[10:11], off offset:2048
	s_nop 0
	global_load_dwordx4 v[2:5], v[2:3], off offset:2304
	s_nop 0
	global_load_dwordx4 v[10:13], v[10:11], off offset:2304
	s_waitcnt vmcnt(6)
	v_lshlrev_b32_e32 v27, 16, v158
	v_lshlrev_b32_e32 v168, 16, v18
	v_and_b32_e32 v169, 0xffff0000, v18
	v_lshlrev_b32_e32 v18, 16, v159
	v_max_f32_e32 v27, v27, v27
	v_max_f32_e32 v18, v18, v18
	v_max_f32_e32 v27, 0xda24260, v27
	v_max_f32_e32 v18, 0xda24260, v18
	v_rcp_f32_e32 v166, v27
	v_and_b32_e32 v27, 0xffff0000, v158
	v_rcp_f32_e32 v158, v18
	v_and_b32_e32 v18, 0xffff0000, v159
	v_max_f32_e32 v18, v18, v18
	v_max_f32_e32 v18, 0xda24260, v18
	v_rcp_f32_e32 v159, v18
	v_lshlrev_b32_e32 v18, 16, v19
	v_and_b32_e32 v19, 0xffff0000, v19
	v_pk_mul_f32 v[18:19], v[18:19], 0.5 op_sel_hi:[1,0]
	v_max_f32_e32 v27, v27, v27
	v_pk_mul_f32 v[18:19], v[18:19], v[158:159]
	v_lshlrev_b32_e32 v158, 16, v20
	v_pk_mul_f32 v[92:93], v[92:93], v[18:19]
	v_lshlrev_b32_e32 v18, 16, v160
	v_and_b32_e32 v19, 0xffff0000, v160
	v_max_f32_e32 v18, v18, v18
	v_max_f32_e32 v19, v19, v19
	v_max_f32_e32 v18, 0xda24260, v18
	v_max_f32_e32 v19, 0xda24260, v19
	v_rcp_f32_e32 v18, v18
	v_rcp_f32_e32 v19, v19
	v_and_b32_e32 v159, 0xffff0000, v20
	v_lshlrev_b32_e32 v20, 16, v161
	v_max_f32_e32 v20, v20, v20
	v_pk_mul_f32 v[158:159], v[158:159], 0.5 op_sel_hi:[1,0]
	v_max_f32_e32 v20, 0xda24260, v20
	v_pk_mul_f32 v[18:19], v[158:159], v[18:19]
	v_rcp_f32_e32 v158, v20
	v_and_b32_e32 v20, 0xffff0000, v161
	v_max_f32_e32 v20, v20, v20
	v_max_f32_e32 v20, 0xda24260, v20
	v_rcp_f32_e32 v159, v20
	v_lshlrev_b32_e32 v20, 16, v21
	v_and_b32_e32 v21, 0xffff0000, v21
	v_pk_mul_f32 v[20:21], v[20:21], 0.5 op_sel_hi:[1,0]
	v_pk_mul_f32 v[86:87], v[86:87], v[18:19]
	v_pk_mul_f32 v[20:21], v[20:21], v[158:159]
	s_waitcnt vmcnt(4)
	v_lshlrev_b32_e32 v18, 16, v14
	v_pk_mul_f32 v[88:89], v[88:89], v[20:21]
	v_and_b32_e32 v14, 0xffff0000, v14
	v_lshlrev_b32_e32 v20, 16, v6
	v_and_b32_e32 v21, 0xffff0000, v6
	v_lshlrev_b32_e32 v6, 16, v15
	v_max_f32_e32 v14, v14, v14
	v_max_f32_e32 v6, v6, v6
	v_max_f32_e32 v14, 0xda24260, v14
	v_max_f32_e32 v6, 0xda24260, v6
	v_rcp_f32_e32 v19, v14
	v_rcp_f32_e32 v14, v6
	v_and_b32_e32 v6, 0xffff0000, v15
	v_max_f32_e32 v6, v6, v6
	v_max_f32_e32 v6, 0xda24260, v6
	v_rcp_f32_e32 v15, v6
	v_lshlrev_b32_e32 v6, 16, v7
	v_and_b32_e32 v7, 0xffff0000, v7
	v_pk_mul_f32 v[6:7], v[6:7], 0.5 op_sel_hi:[1,0]
	v_max_f32_e32 v27, 0xda24260, v27
	v_pk_mul_f32 v[6:7], v[6:7], v[14:15]
	v_lshlrev_b32_e32 v14, 16, v8
	v_pk_mul_f32 v[84:85], v[84:85], v[6:7]
	v_lshlrev_b32_e32 v6, 16, v16
	v_and_b32_e32 v7, 0xffff0000, v16
	v_max_f32_e32 v6, v6, v6
	v_max_f32_e32 v7, v7, v7
	v_max_f32_e32 v6, 0xda24260, v6
	v_max_f32_e32 v7, 0xda24260, v7
	v_rcp_f32_e32 v6, v6
	v_rcp_f32_e32 v7, v7
	v_and_b32_e32 v15, 0xffff0000, v8
	v_lshlrev_b32_e32 v8, 16, v17
	v_max_f32_e32 v8, v8, v8
	v_rcp_f32_e32 v167, v27
	v_pk_mul_f32 v[14:15], v[14:15], 0.5 op_sel_hi:[1,0]
	v_max_f32_e32 v8, 0xda24260, v8
	v_max_f32_e32 v18, v18, v18
	v_pk_mul_f32 v[6:7], v[14:15], v[6:7]
	v_rcp_f32_e32 v14, v8
	v_and_b32_e32 v8, 0xffff0000, v17
	v_max_f32_e32 v18, 0xda24260, v18
	v_max_f32_e32 v8, v8, v8
	v_pk_mul_f32 v[168:169], v[168:169], 0.5 op_sel_hi:[1,0]
	v_rcp_f32_e32 v18, v18
	v_max_f32_e32 v8, 0xda24260, v8
	v_pk_mul_f32 v[166:167], v[168:169], v[166:167]
	v_rcp_f32_e32 v15, v8
	s_waitcnt vmcnt(2)
; #define MG_LOAD(G_, s_) do { const bf16* q_ = pb + (size_t)(((s_) >> 2) * 128 + ((s_) & 3) * 16) * PNP; G_[0] = *(const GAS v4u*)(q_ + PGA); G_[1] = *(const GAS v4u*)(q_ + PGB); G_[2] = *(const GAS v4u*)(q_ + PGA + 128); G_[3] = *(const GAS v4u*)(q_ + PGB + 128); } while (0)
;     __device__ __forceinline__ void mid(f32x4 (&acc)[2][2][4][2], const Unit& u, int wr, int wc, int fr, int fq) const {
;     ...
;         MG_LOAD(A0, 0); MG_LOAD(A1, 1); MG_APPLY(A0, 0); MG_LOAD(A0, 2); MG_APPLY(A1, 1); MG_LOAD(A1, 3); MG_APPLY(A0, 2); MG_LOAD(A0, 4); MG_APPLY(A1, 3); MG_LOAD(A1, 5);
;         MG_APPLY(A0, 4); MG_LOAD(A0, 6); MG_APPLY(A1, 5); MG_LOAD(A1, 7); MG_APPLY(A0, 6); MG_APPLY(A1, 7);
	v_lshlrev_b32_e32 v27, 16, v162
	v_lshlrev_b32_e32 v168, 16, v22
	v_and_b32_e32 v169, 0xffff0000, v22
	v_lshlrev_b32_e32 v22, 16, v163
	s_mov_b32 s34, 0x568000
	v_max_f32_e32 v27, v27, v27
	v_max_f32_e32 v22, v22, v22
	v_pk_mul_f32 v[20:21], v[20:21], 0.5 op_sel_hi:[1,0]
	v_lshlrev_b32_e32 v8, 16, v9
	v_and_b32_e32 v9, 0xffff0000, v9
	v_pk_mul_f32 v[78:79], v[78:79], v[6:7]
	v_add_co_u32_e32 v6, vcc, s34, v28
	v_max_f32_e32 v27, 0xda24260, v27
	v_max_f32_e32 v22, 0xda24260, v22
	v_pk_mul_f32 v[90:91], v[90:91], v[166:167]
	v_pk_mul_f32 v[18:19], v[20:21], v[18:19]
	v_pk_mul_f32 v[8:9], v[8:9], 0.5 op_sel_hi:[1,0]
	v_addc_co_u32_e32 v7, vcc, 0, v29, vcc
	s_mov_b32 s34, 0x56a000
	v_rcp_f32_e32 v166, v27
	v_and_b32_e32 v27, 0xffff0000, v162
	v_rcp_f32_e32 v162, v22
	v_and_b32_e32 v22, 0xffff0000, v163
	v_pk_mul_f32 v[82:83], v[82:83], v[18:19]
	v_pk_mul_f32 v[8:9], v[8:9], v[14:15]
	global_load_dwordx4 v[18:21], v[6:7], off offset:2048
	v_add_co_u32_e32 v14, vcc, s34, v28
	v_max_f32_e32 v22, v22, v22
	s_nop 0
	v_addc_co_u32_e32 v15, vcc, 0, v29, vcc
	v_max_f32_e32 v22, 0xda24260, v22
	v_pk_mul_f32 v[80:81], v[80:81], v[8:9]
	global_load_dwordx4 v[158:161], v[14:15], off offset:2048
	s_nop 0
	global_load_dwordx4 v[6:9], v[6:7], off offset:2304
	s_nop 0
	global_load_dwordx4 v[14:17], v[14:15], off offset:2304
	v_rcp_f32_e32 v163, v22
	v_lshlrev_b32_e32 v22, 16, v23
	v_and_b32_e32 v23, 0xffff0000, v23
	v_pk_mul_f32 v[22:23], v[22:23], 0.5 op_sel_hi:[1,0]
	s_mov_b32 s34, 0x5f2000
	v_pk_mul_f32 v[22:23], v[22:23], v[162:163]
	v_lshlrev_b32_e32 v162, 16, v24
	v_pk_mul_f32 v[76:77], v[76:77], v[22:23]
	v_lshlrev_b32_e32 v22, 16, v164
	v_and_b32_e32 v23, 0xffff0000, v164
	v_max_f32_e32 v22, v22, v22
	v_max_f32_e32 v23, v23, v23
	v_max_f32_e32 v22, 0xda24260, v22
	v_max_f32_e32 v23, 0xda24260, v23
	v_rcp_f32_e32 v22, v22
	v_rcp_f32_e32 v23, v23
	v_and_b32_e32 v163, 0xffff0000, v24
	v_lshlrev_b32_e32 v24, 16, v165
	v_max_f32_e32 v24, v24, v24
	v_pk_mul_f32 v[162:163], v[162:163], 0.5 op_sel_hi:[1,0]
	v_max_f32_e32 v24, 0xda24260, v24
	v_pk_mul_f32 v[22:23], v[162:163], v[22:23]
	v_rcp_f32_e32 v162, v24
	v_and_b32_e32 v24, 0xffff0000, v165
	v_max_f32_e32 v24, v24, v24
	v_max_f32_e32 v24, 0xda24260, v24
	v_rcp_f32_e32 v163, v24
	v_lshlrev_b32_e32 v24, 16, v25
	v_and_b32_e32 v25, 0xffff0000, v25
	v_pk_mul_f32 v[24:25], v[24:25], 0.5 op_sel_hi:[1,0]
	v_pk_mul_f32 v[70:71], v[70:71], v[22:23]
	v_pk_mul_f32 v[24:25], v[24:25], v[162:163]
	s_waitcnt vmcnt(4)
	v_lshlrev_b32_e32 v22, 16, v10
	v_pk_mul_f32 v[72:73], v[72:73], v[24:25]
	v_and_b32_e32 v10, 0xffff0000, v10
	v_lshlrev_b32_e32 v24, 16, v2
	v_and_b32_e32 v25, 0xffff0000, v2
	v_lshlrev_b32_e32 v2, 16, v11
	v_max_f32_e32 v10, v10, v10
	v_max_f32_e32 v2, v2, v2
	v_max_f32_e32 v10, 0xda24260, v10
	v_max_f32_e32 v2, 0xda24260, v2
	v_rcp_f32_e32 v23, v10
	v_rcp_f32_e32 v10, v2
	v_and_b32_e32 v2, 0xffff0000, v11
	v_max_f32_e32 v2, v2, v2
	v_max_f32_e32 v2, 0xda24260, v2
	v_rcp_f32_e32 v11, v2
	v_lshlrev_b32_e32 v2, 16, v3
	v_and_b32_e32 v3, 0xffff0000, v3
	v_pk_mul_f32 v[2:3], v[2:3], 0.5 op_sel_hi:[1,0]
	v_max_f32_e32 v22, v22, v22
	v_pk_mul_f32 v[2:3], v[2:3], v[10:11]
	v_lshlrev_b32_e32 v10, 16, v4
	v_pk_mul_f32 v[68:69], v[68:69], v[2:3]
	v_lshlrev_b32_e32 v2, 16, v12
	v_and_b32_e32 v3, 0xffff0000, v12
	v_max_f32_e32 v2, v2, v2
	v_max_f32_e32 v3, v3, v3
	v_max_f32_e32 v2, 0xda24260, v2
	v_max_f32_e32 v3, 0xda24260, v3
	v_rcp_f32_e32 v2, v2
	v_rcp_f32_e32 v3, v3
	v_and_b32_e32 v11, 0xffff0000, v4
	v_lshlrev_b32_e32 v4, 16, v13
	v_max_f32_e32 v4, v4, v4
	v_pk_mul_f32 v[10:11], v[10:11], 0.5 op_sel_hi:[1,0]
	v_max_f32_e32 v4, 0xda24260, v4
	v_pk_mul_f32 v[2:3], v[10:11], v[2:3]
	v_rcp_f32_e32 v10, v4
	v_and_b32_e32 v4, 0xffff0000, v13
	v_max_f32_e32 v4, v4, v4
	v_max_f32_e32 v4, 0xda24260, v4
	v_max_f32_e32 v22, 0xda24260, v22
	v_rcp_f32_e32 v11, v4
	v_rcp_f32_e32 v22, v22
	v_lshlrev_b32_e32 v4, 16, v5
	v_and_b32_e32 v5, 0xffff0000, v5
	v_pk_mul_f32 v[62:63], v[62:63], v[2:3]
	v_add_co_u32_e32 v2, vcc, s34, v28
	v_pk_mul_f32 v[4:5], v[4:5], 0.5 op_sel_hi:[1,0]
	s_nop 0
	v_addc_co_u32_e32 v3, vcc, 0, v29, vcc
	s_mov_b32 s34, 0x5f4000
	v_pk_mul_f32 v[24:25], v[24:25], 0.5 op_sel_hi:[1,0]
	v_pk_mul_f32 v[4:5], v[4:5], v[10:11]
	v_add_co_u32_e32 v10, vcc, s34, v28
	v_pk_mul_f32 v[22:23], v[24:25], v[22:23]
	s_nop 0
	v_addc_co_u32_e32 v11, vcc, 0, v29, vcc
	v_pk_mul_f32 v[66:67], v[66:67], v[22:23]
	v_pk_mul_f32 v[64:65], v[64:65], v[4:5]
	global_load_dwordx4 v[22:25], v[2:3], off offset:2048
	global_load_dwordx4 v[162:165], v[10:11], off offset:2048
	s_nop 0
	global_load_dwordx4 v[2:5], v[2:3], off offset:2304
	s_nop 0
	global_load_dwordx4 v[10:13], v[10:11], off offset:2304
	v_max_f32_e32 v27, v27, v27
	v_max_f32_e32 v27, 0xda24260, v27
	v_rcp_f32_e32 v167, v27
	v_pk_mul_f32 v[168:169], v[168:169], 0.5 op_sel_hi:[1,0]
	s_waitcnt vmcnt(6)
; #define MG_LOAD(G_, s_) do { const bf16* q_ = pb + (size_t)(((s_) >> 2) * 128 + ((s_) & 3) * 16) * PNP; G_[0] = *(const GAS v4u*)(q_ + PGA); G_[1] = *(const GAS v4u*)(q_ + PGB); G_[2] = *(const GAS v4u*)(q_ + PGA + 128); G_[3] = *(const GAS v4u*)(q_ + PGB + 128); } while (0)
;     __device__ __forceinline__ void mid(f32x4 (&acc)[2][2][4][2], const Unit& u, int wr, int wc, int fr, int fq) const {
;     ...
;         MG_LOAD(A0, 0); MG_LOAD(A1, 1); MG_APPLY(A0, 0); MG_LOAD(A0, 2); MG_APPLY(A1, 1); MG_LOAD(A1, 3); MG_APPLY(A0, 2); MG_LOAD(A0, 4); MG_APPLY(A1, 3); MG_LOAD(A1, 5);
;         MG_APPLY(A0, 4); MG_LOAD(A0, 6); MG_APPLY(A1, 5); MG_LOAD(A1, 7); MG_APPLY(A0, 6); MG_APPLY(A1, 7);
	v_lshlrev_b32_e32 v27, 16, v158
	v_max_f32_e32 v27, v27, v27
	v_pk_mul_f32 v[166:167], v[168:169], v[166:167]
	v_max_f32_e32 v27, 0xda24260, v27
	v_pk_mul_f32 v[74:75], v[74:75], v[166:167]
	v_lshlrev_b32_e32 v166, 16, v18
	v_and_b32_e32 v167, 0xffff0000, v18
	v_lshlrev_b32_e32 v18, 16, v159
	v_max_f32_e32 v18, v18, v18
	v_max_f32_e32 v18, 0xda24260, v18
	v_rcp_f32_e32 v28, v27
	v_and_b32_e32 v27, 0xffff0000, v158
	v_rcp_f32_e32 v158, v18
	v_and_b32_e32 v18, 0xffff0000, v159
	v_max_f32_e32 v18, v18, v18
	v_max_f32_e32 v18, 0xda24260, v18
	v_rcp_f32_e32 v159, v18
	v_max_f32_e32 v27, v27, v27
	v_lshlrev_b32_e32 v18, 16, v19
	v_and_b32_e32 v19, 0xffff0000, v19
	v_max_f32_e32 v27, 0xda24260, v27
	v_pk_mul_f32 v[18:19], v[18:19], 0.5 op_sel_hi:[1,0]
	v_rcp_f32_e32 v29, v27
	v_pk_mul_f32 v[18:19], v[18:19], v[158:159]
	v_pk_mul_f32 v[166:167], v[166:167], 0.5 op_sel_hi:[1,0]
	v_pk_mul_f32 v[60:61], v[60:61], v[18:19]
	v_lshlrev_b32_e32 v18, 16, v160
	v_and_b32_e32 v19, 0xffff0000, v160
	v_max_f32_e32 v18, v18, v18
	v_max_f32_e32 v19, v19, v19
	v_max_f32_e32 v18, 0xda24260, v18
	v_max_f32_e32 v19, 0xda24260, v19
	v_pk_mul_f32 v[28:29], v[166:167], v[28:29]
	v_rcp_f32_e32 v18, v18
	v_rcp_f32_e32 v19, v19
	v_pk_mul_f32 v[58:59], v[58:59], v[28:29]
	v_lshlrev_b32_e32 v28, 16, v20
	v_and_b32_e32 v29, 0xffff0000, v20
	v_lshlrev_b32_e32 v20, 16, v161
	v_max_f32_e32 v20, v20, v20
	v_pk_mul_f32 v[28:29], v[28:29], 0.5 op_sel_hi:[1,0]
	v_max_f32_e32 v20, 0xda24260, v20
	v_pk_mul_f32 v[18:19], v[28:29], v[18:19]
	v_rcp_f32_e32 v28, v20
	v_and_b32_e32 v20, 0xffff0000, v161
	v_max_f32_e32 v20, v20, v20
	v_max_f32_e32 v20, 0xda24260, v20
	v_rcp_f32_e32 v29, v20
	v_lshlrev_b32_e32 v20, 16, v21
	v_and_b32_e32 v21, 0xffff0000, v21
	v_pk_mul_f32 v[20:21], v[20:21], 0.5 op_sel_hi:[1,0]
	v_pk_mul_f32 v[54:55], v[54:55], v[18:19]
	v_pk_mul_f32 v[20:21], v[20:21], v[28:29]
	s_waitcnt vmcnt(4)
	v_lshlrev_b32_e32 v18, 16, v14
	v_pk_mul_f32 v[56:57], v[56:57], v[20:21]
	v_and_b32_e32 v14, 0xffff0000, v14
	v_lshlrev_b32_e32 v20, 16, v6
	v_and_b32_e32 v21, 0xffff0000, v6
	v_lshlrev_b32_e32 v6, 16, v15
	v_max_f32_e32 v14, v14, v14
	v_max_f32_e32 v6, v6, v6
	v_max_f32_e32 v14, 0xda24260, v14
	v_max_f32_e32 v6, 0xda24260, v6
	v_rcp_f32_e32 v19, v14
	v_rcp_f32_e32 v14, v6
	v_and_b32_e32 v6, 0xffff0000, v15
	v_max_f32_e32 v6, v6, v6
	v_max_f32_e32 v6, 0xda24260, v6
	v_rcp_f32_e32 v15, v6
	v_lshlrev_b32_e32 v6, 16, v7
	v_and_b32_e32 v7, 0xffff0000, v7
	v_pk_mul_f32 v[6:7], v[6:7], 0.5 op_sel_hi:[1,0]
	v_max_f32_e32 v18, v18, v18
	v_pk_mul_f32 v[6:7], v[6:7], v[14:15]
	v_lshlrev_b32_e32 v14, 16, v8
	v_pk_mul_f32 v[52:53], v[52:53], v[6:7]
	v_lshlrev_b32_e32 v6, 16, v16
	v_and_b32_e32 v7, 0xffff0000, v16
	v_max_f32_e32 v6, v6, v6
	v_max_f32_e32 v7, v7, v7
	v_max_f32_e32 v6, 0xda24260, v6
	v_max_f32_e32 v7, 0xda24260, v7
	v_rcp_f32_e32 v6, v6
	v_rcp_f32_e32 v7, v7
	v_and_b32_e32 v15, 0xffff0000, v8
	v_lshlrev_b32_e32 v8, 16, v17
	v_max_f32_e32 v8, v8, v8
	v_pk_mul_f32 v[14:15], v[14:15], 0.5 op_sel_hi:[1,0]
	v_max_f32_e32 v8, 0xda24260, v8
	v_pk_mul_f32 v[6:7], v[14:15], v[6:7]
	v_rcp_f32_e32 v14, v8
	v_and_b32_e32 v8, 0xffff0000, v17
	v_max_f32_e32 v8, v8, v8
	v_max_f32_e32 v8, 0xda24260, v8
	v_rcp_f32_e32 v15, v8
	v_pk_mul_f32 v[46:47], v[46:47], v[6:7]
	s_waitcnt vmcnt(2)
; #define MG_LOAD(G_, s_) do { const bf16* q_ = pb + (size_t)(((s_) >> 2) * 128 + ((s_) & 3) * 16) * PNP; G_[0] = *(const GAS v4u*)(q_ + PGA); G_[1] = *(const GAS v4u*)(q_ + PGB); G_[2] = *(const GAS v4u*)(q_ + PGA + 128); G_[3] = *(const GAS v4u*)(q_ + PGB + 128); } while (0)
;     __device__ __forceinline__ void mid(f32x4 (&acc)[2][2][4][2], const Unit& u, int wr, int wc, int fr, int fq) const {
;     ...
;         MG_LOAD(A0, 0); MG_LOAD(A1, 1); MG_APPLY(A0, 0); MG_LOAD(A0, 2); MG_APPLY(A1, 1); MG_LOAD(A1, 3); MG_APPLY(A0, 2); MG_LOAD(A0, 4); MG_APPLY(A1, 3); MG_LOAD(A1, 5);
;         MG_APPLY(A0, 4); MG_LOAD(A0, 6); MG_APPLY(A1, 5); MG_LOAD(A1, 7); MG_APPLY(A0, 6); MG_APPLY(A1, 7);
	v_lshlrev_b32_e32 v6, 16, v162
	v_and_b32_e32 v7, 0xffff0000, v162
	v_max_f32_e32 v6, v6, v6
	v_max_f32_e32 v7, v7, v7
	v_lshlrev_b32_e32 v8, 16, v9
	v_and_b32_e32 v9, 0xffff0000, v9
	v_max_f32_e32 v6, 0xda24260, v6
	v_max_f32_e32 v7, 0xda24260, v7
	v_pk_mul_f32 v[8:9], v[8:9], 0.5 op_sel_hi:[1,0]
	v_rcp_f32_e32 v6, v6
	v_rcp_f32_e32 v7, v7
	v_pk_mul_f32 v[8:9], v[8:9], v[14:15]
	v_lshlrev_b32_e32 v14, 16, v23
	v_pk_mul_f32 v[48:49], v[48:49], v[8:9]
	v_lshlrev_b32_e32 v8, 16, v22
	v_and_b32_e32 v9, 0xffff0000, v22
	v_pk_mul_f32 v[8:9], v[8:9], 0.5 op_sel_hi:[1,0]
	v_and_b32_e32 v15, 0xffff0000, v23
	v_pk_mul_f32 v[6:7], v[8:9], v[6:7]
	v_lshlrev_b32_e32 v8, 16, v163
	v_and_b32_e32 v9, 0xffff0000, v163
	v_max_f32_e32 v8, v8, v8
	v_max_f32_e32 v9, v9, v9
	v_max_f32_e32 v8, 0xda24260, v8
	v_max_f32_e32 v9, 0xda24260, v9
	v_rcp_f32_e32 v8, v8
	v_rcp_f32_e32 v9, v9
	v_pk_mul_f32 v[42:43], v[42:43], v[6:7]
	v_lshlrev_b32_e32 v6, 16, v164
	v_and_b32_e32 v7, 0xffff0000, v164
	v_max_f32_e32 v6, v6, v6
	v_max_f32_e32 v7, v7, v7
	v_max_f32_e32 v6, 0xda24260, v6
	v_max_f32_e32 v7, 0xda24260, v7
	v_pk_mul_f32 v[14:15], v[14:15], 0.5 op_sel_hi:[1,0]
	v_rcp_f32_e32 v6, v6
	v_rcp_f32_e32 v7, v7
	v_pk_mul_f32 v[8:9], v[14:15], v[8:9]
	v_lshlrev_b32_e32 v14, 16, v25
	v_pk_mul_f32 v[44:45], v[44:45], v[8:9]
	v_lshlrev_b32_e32 v8, 16, v24
	v_and_b32_e32 v9, 0xffff0000, v24
	v_pk_mul_f32 v[8:9], v[8:9], 0.5 op_sel_hi:[1,0]
	v_and_b32_e32 v15, 0xffff0000, v25
	v_pk_mul_f32 v[6:7], v[8:9], v[6:7]
	v_lshlrev_b32_e32 v8, 16, v165
	v_and_b32_e32 v9, 0xffff0000, v165
	v_max_f32_e32 v8, v8, v8
	v_max_f32_e32 v9, v9, v9
	v_max_f32_e32 v8, 0xda24260, v8
	v_max_f32_e32 v9, 0xda24260, v9
	v_rcp_f32_e32 v8, v8
	v_rcp_f32_e32 v9, v9
	v_pk_mul_f32 v[38:39], v[38:39], v[6:7]
	s_waitcnt vmcnt(0)
	v_lshlrev_b32_e32 v6, 16, v10
	v_and_b32_e32 v7, 0xffff0000, v10
	v_max_f32_e32 v6, v6, v6
	v_max_f32_e32 v7, v7, v7
	v_pk_mul_f32 v[14:15], v[14:15], 0.5 op_sel_hi:[1,0]
	v_max_f32_e32 v6, 0xda24260, v6
	v_max_f32_e32 v7, 0xda24260, v7
	v_pk_mul_f32 v[8:9], v[14:15], v[8:9]
	v_rcp_f32_e32 v6, v6
	v_rcp_f32_e32 v7, v7
	v_pk_mul_f32 v[40:41], v[40:41], v[8:9]
	v_lshlrev_b32_e32 v8, 16, v2
	v_and_b32_e32 v9, 0xffff0000, v2
	v_lshlrev_b32_e32 v2, 16, v11
	v_max_f32_e32 v2, v2, v2
	v_pk_mul_f32 v[8:9], v[8:9], 0.5 op_sel_hi:[1,0]
	v_max_f32_e32 v2, 0xda24260, v2
	v_pk_mul_f32 v[6:7], v[8:9], v[6:7]
	v_rcp_f32_e32 v8, v2
	v_and_b32_e32 v2, 0xffff0000, v11
	v_max_f32_e32 v2, v2, v2
	v_max_f32_e32 v2, 0xda24260, v2
	v_rcp_f32_e32 v9, v2
	v_lshlrev_b32_e32 v2, 16, v3
	v_and_b32_e32 v3, 0xffff0000, v3
	v_pk_mul_f32 v[2:3], v[2:3], 0.5 op_sel_hi:[1,0]
	v_pk_mul_f32 v[34:35], v[34:35], v[6:7]
	v_pk_mul_f32 v[2:3], v[2:3], v[8:9]
	v_lshlrev_b32_e32 v6, 16, v4
	v_pk_mul_f32 v[36:37], v[36:37], v[2:3]
	v_lshlrev_b32_e32 v2, 16, v12
	v_and_b32_e32 v3, 0xffff0000, v12
	v_max_f32_e32 v2, v2, v2
	v_max_f32_e32 v3, v3, v3
	v_max_f32_e32 v2, 0xda24260, v2
	v_max_f32_e32 v3, 0xda24260, v3
	v_rcp_f32_e32 v2, v2
	v_rcp_f32_e32 v3, v3
	v_and_b32_e32 v7, 0xffff0000, v4
	v_lshlrev_b32_e32 v4, 16, v13
	v_max_f32_e32 v4, v4, v4
	v_pk_mul_f32 v[6:7], v[6:7], 0.5 op_sel_hi:[1,0]
	v_max_f32_e32 v4, 0xda24260, v4
	v_pk_mul_f32 v[2:3], v[6:7], v[2:3]
	v_rcp_f32_e32 v6, v4
	v_and_b32_e32 v4, 0xffff0000, v13
	v_max_f32_e32 v4, v4, v4
	v_max_f32_e32 v18, 0xda24260, v18
	v_max_f32_e32 v4, 0xda24260, v4
	v_rcp_f32_e32 v18, v18
	v_rcp_f32_e32 v7, v4
	v_lshlrev_b32_e32 v4, 16, v5
	v_and_b32_e32 v5, 0xffff0000, v5
	v_pk_mul_f32 v[20:21], v[20:21], 0.5 op_sel_hi:[1,0]
	v_pk_mul_f32 v[4:5], v[4:5], 0.5 op_sel_hi:[1,0]
	v_pk_mul_f32 v[18:19], v[20:21], v[18:19]
	v_pk_mul_f32 v[4:5], v[4:5], v[6:7]
	v_pk_mul_f32 v[50:51], v[50:51], v[18:19]
	v_pk_mul_f32 v[32:33], v[32:33], v[4:5]
	v_pk_mul_f32 v[30:31], v[30:31], v[2:3]
	s_branch .LBB0_1708
